# weight conversion: f32 weight tile loads marked nt (read once, no cache allocation)
# speedup vs baseline: 1.0104x; 1.0104x over previous
.LBB0_85:
	s_movk_i32 s0, 0x6cf
	v_cmp_lt_i32_e32 vcc, s0, v46
	s_and_saveexec_b64 s[0:1], vcc
	s_xor_b64 s[0:1], exec, s[0:1]
	s_cbranch_execz .LBB0_99
	s_movk_i32 s40, 0x84f
	v_cmp_lt_u32_e32 vcc, s40, v46
	s_and_saveexec_b64 s[42:43], vcc
	s_xor_b64 s[46:47], exec, s[42:43]
	s_cbranch_execz .LBB0_96
	s_movk_i32 s40, 0x94f
	v_cmp_lt_u32_e32 vcc, s40, v46
	s_and_saveexec_b64 s[42:43], vcc
	s_xor_b64 s[48:49], exec, s[42:43]
	s_cbranch_execz .LBB0_93
	s_movk_i32 s42, 0x494f
	v_cmp_lt_u32_e32 vcc, s42, v46
	s_and_saveexec_b64 s[42:43], vcc
	s_xor_b64 s[50:51], exec, s[42:43]
	s_cbranch_execz .LBB0_90
	v_add_u32_e32 v4, 0xffffb6b0, v46
	v_add_u32_e32 v6, 0xffedac00, v3
	v_lshrrev_b32_e32 v130, 9, v4
	v_and_b32_e32 v47, 0x7c0, v6
	v_lshlrev_b64 v[4:5], 23, v[130:131]
	v_and_b32_e32 v76, 0x3c0, v45
	v_or_b32_e32 v7, v47, v123
	v_lshl_add_u64 v[4:5], s[18:19], 0, v[4:5]
	v_lshlrev_b64 v[40:41], 22, v[130:131]
	v_or_b32_e32 v6, v76, v162
	v_lshlrev_b32_e32 v130, 12, v7
	v_lshl_add_u64 v[4:5], v[4:5], 0, v[130:131]
	v_lshlrev_b32_e32 v130, 2, v6
	v_lshl_add_u64 v[68:69], v[4:5], 0, v[130:131]
	s_waitcnt lgkmcnt(0)
	v_add_co_u32_e32 v8, vcc, s88, v68
	s_mov_b32 s41, 0x8000
	s_nop 0
	v_addc_co_u32_e32 v9, vcc, 0, v69, vcc
	v_add_co_u32_e32 v12, vcc, s41, v68
	s_mov_b32 s43, 0x10000
	s_nop 0
	v_addc_co_u32_e32 v13, vcc, 0, v69, vcc
	v_add_co_u32_e32 v16, vcc, s82, v68
	s_mov_b32 s40, 0x14000
	s_nop 0
	v_addc_co_u32_e32 v17, vcc, 0, v69, vcc
	v_add_co_u32_e32 v20, vcc, s43, v68
	s_mov_b32 s42, 0x18000
	s_nop 0
	v_addc_co_u32_e32 v21, vcc, 0, v69, vcc
	v_add_co_u32_e32 v24, vcc, s40, v68
	s_mov_b32 s40, 0x1c000
	s_nop 0
	v_addc_co_u32_e32 v25, vcc, 0, v69, vcc
	v_add_co_u32_e32 v28, vcc, s42, v68
	s_mov_b32 s44, 0x24000
	s_nop 0
	v_addc_co_u32_e32 v29, vcc, 0, v69, vcc
	v_add_co_u32_e32 v32, vcc, s40, v68
	s_mov_b32 s40, 0x20000
	s_nop 0
	v_addc_co_u32_e32 v33, vcc, 0, v69, vcc
	v_add_co_u32_e32 v36, vcc, s40, v68
	s_mov_b32 s45, 0x2c000
	s_nop 0
	v_addc_co_u32_e32 v37, vcc, 0, v69, vcc
	v_add_co_u32_e32 v48, vcc, s44, v68
	s_mov_b32 s44, 0x28000
	s_nop 0
	v_addc_co_u32_e32 v49, vcc, 0, v69, vcc
	v_add_co_u32_e32 v52, vcc, s44, v68
	s_mov_b32 s52, 0x34000
	s_nop 0
	v_addc_co_u32_e32 v53, vcc, 0, v69, vcc
	v_add_co_u32_e32 v56, vcc, s45, v68
	s_mov_b32 s45, 0x30000
	s_nop 0
	v_addc_co_u32_e32 v57, vcc, 0, v69, vcc
	v_add_co_u32_e32 v60, vcc, s45, v68
	global_load_dwordx4 v[4:7], v[68:69], off nt
	s_nop 0
	global_load_dwordx4 v[8:11], v[8:9], off nt
	v_addc_co_u32_e32 v61, vcc, 0, v69, vcc
	v_add_co_u32_e32 v64, vcc, s52, v68
	s_mov_b32 s52, 0x38000
	s_nop 0
	v_addc_co_u32_e32 v65, vcc, 0, v69, vcc
	v_add_co_u32_e32 v70, vcc, s52, v68
	s_mov_b32 s52, 0x3c000
	s_nop 0
	v_addc_co_u32_e32 v71, vcc, 0, v69, vcc
	v_add_co_u32_e32 v72, vcc, s52, v68
	global_load_dwordx4 v[12:15], v[12:13], off nt
	s_nop 0
	global_load_dwordx4 v[16:19], v[16:17], off nt
	v_addc_co_u32_e32 v73, vcc, 0, v69, vcc
	global_load_dwordx4 v[20:23], v[20:21], off nt
	s_nop 0
	global_load_dwordx4 v[24:27], v[24:25], off nt
	s_nop 0
	global_load_dwordx4 v[28:31], v[28:29], off nt
	s_nop 0
	global_load_dwordx4 v[32:35], v[32:33], off nt
	s_nop 0
	global_load_dwordx4 v[36:39], v[36:37], off nt
	s_nop 0
	global_load_dwordx4 v[48:51], v[48:49], off nt
	s_nop 0
	global_load_dwordx4 v[52:55], v[52:53], off nt
	s_nop 0
	global_load_dwordx4 v[56:59], v[56:57], off nt
	s_nop 0
	global_load_dwordx4 v[60:63], v[60:61], off nt
	s_nop 0
	global_load_dwordx4 v[64:67], v[64:65], off nt
	s_nop 0
	global_load_dwordx4 v[68:71], v[70:71], off nt
	s_nop 0
	global_load_dwordx4 v[72:75], v[72:73], off nt
	v_lshl_add_u64 v[40:41], s[78:79], 0, v[40:41]
	s_waitcnt vmcnt(0)
	ds_write2_b32 v163, v4, v5 offset1:1
	ds_write2_b32 v163, v6, v7 offset0:2 offset1:3
	v_add_u32_e32 v4, 0x410, v163
	ds_write2_b32 v4, v8, v9 offset1:1
	v_add_u32_e32 v4, 0x418, v163
	ds_write2_b32 v4, v10, v11 offset1:1
	v_add_u32_e32 v4, 0x820, v163
	ds_write2_b32 v4, v12, v13 offset1:1
	v_add_u32_e32 v4, 0x828, v163
	ds_write2_b32 v4, v14, v15 offset1:1
	v_add_u32_e32 v4, 0xc30, v163
	ds_write2_b32 v4, v16, v17 offset1:1
	v_add_u32_e32 v4, 0xc38, v163
	ds_write2_b32 v4, v18, v19 offset1:1
	v_add_u32_e32 v4, 0x1040, v163
	ds_write2_b32 v4, v20, v21 offset1:1
	v_add_u32_e32 v4, 0x1048, v163
	ds_write2_b32 v4, v22, v23 offset1:1
	v_add_u32_e32 v4, 0x1450, v163
	ds_write2_b32 v4, v24, v25 offset1:1
	v_add_u32_e32 v4, 0x1458, v163
	ds_write2_b32 v4, v26, v27 offset1:1
	v_add_u32_e32 v4, 0x1860, v163
	ds_write2_b32 v4, v28, v29 offset1:1
	v_add_u32_e32 v4, 0x1868, v163
	ds_write2_b32 v4, v30, v31 offset1:1
	v_add_u32_e32 v4, 0x1c70, v163
	ds_write2_b32 v4, v32, v33 offset1:1
	v_add_u32_e32 v4, 0x1c78, v163
	ds_write2_b32 v4, v34, v35 offset1:1
	v_add_u32_e32 v4, 0x2080, v163
	ds_write2_b32 v4, v36, v37 offset1:1
	v_add_u32_e32 v4, 0x2088, v163
	ds_write2_b32 v4, v38, v39 offset1:1
	v_add_u32_e32 v4, 0x2490, v163
	ds_write2_b32 v4, v48, v49 offset1:1
	v_add_u32_e32 v4, 0x2498, v163
	ds_write2_b32 v4, v50, v51 offset1:1
	v_add_u32_e32 v4, 0x28a0, v163
	ds_write2_b32 v4, v52, v53 offset1:1
	v_add_u32_e32 v4, 0x28a8, v163
	ds_write2_b32 v4, v54, v55 offset1:1
	v_add_u32_e32 v4, 0x2cb0, v163
	ds_write2_b32 v4, v56, v57 offset1:1
	v_add_u32_e32 v4, 0x2cb8, v163
	ds_write2_b32 v4, v58, v59 offset1:1
	v_add_u32_e32 v4, 0x30c0, v163
	ds_write2_b32 v4, v60, v61 offset1:1
	v_add_u32_e32 v4, 0x30c8, v163
	ds_write2_b32 v4, v62, v63 offset1:1
	v_add_u32_e32 v4, 0x34d0, v163
	ds_write2_b32 v4, v64, v65 offset1:1
	v_add_u32_e32 v4, 0x34d8, v163
	ds_write2_b32 v4, v66, v67 offset1:1
	v_add_u32_e32 v4, 0x38e0, v163
	ds_write2_b32 v4, v68, v69 offset1:1
	v_add_u32_e32 v4, 0x38e8, v163
	ds_write2_b32 v4, v70, v71 offset1:1
	v_add_u32_e32 v4, 0x3cf0, v163
	ds_write2_b32 v4, v72, v73 offset1:1
	v_add_u32_e32 v4, 0x3cf8, v163
	ds_write2_b32 v4, v74, v75 offset1:1
	v_add_u32_e32 v49, 0x400, v165
	ds_read2_b32 v[8:9], v165 offset0:65 offset1:73
	ds_read2_b32 v[10:11], v165 offset0:130 offset1:138
	ds_read2_b32 v[12:13], v165 offset0:195 offset1:203
	ds_read2_b32 v[14:15], v49 offset0:4 offset1:12
	ds_read2_b32 v[16:17], v49 offset0:69 offset1:77
	ds_read2_b32 v[18:19], v49 offset0:134 offset1:142
	ds_read2_b32 v[20:21], v49 offset0:199 offset1:207
	ds_read2_b32 v[22:23], v165 offset1:8
	ds_read2_b32 v[24:25], v165 offset0:16 offset1:24
	ds_read2_b32 v[26:27], v165 offset0:81 offset1:89
	ds_read2_b32 v[28:29], v165 offset0:146 offset1:154
	ds_read2_b32 v[30:31], v165 offset0:211 offset1:219
	ds_read2_b32 v[32:33], v49 offset0:20 offset1:28
	ds_read2_b32 v[34:35], v49 offset0:85 offset1:93
	ds_read2_b32 v[36:37], v49 offset0:150 offset1:158
	ds_read2_b32 v[38:39], v49 offset0:215 offset1:223
	v_lshlrev_b32_e32 v130, 1, v47
	v_lshl_add_u64 v[4:5], v[40:41], 0, v[130:131]
	v_lshlrev_b32_e32 v130, 1, v116
	v_or_b32_e32 v48, v76, v164
	v_lshl_add_u64 v[40:41], v[4:5], 0, v[130:131]
	v_lshlrev_b32_e32 v130, 12, v48
	v_lshl_add_u64 v[40:41], v[40:41], 0, v[130:131]
	s_waitcnt lgkmcnt(8)
	v_cvt_pk_bf16_f32 v4, v22, v8
	v_cvt_pk_bf16_f32 v5, v10, v12
	v_cvt_pk_bf16_f32 v6, v14, v16
	v_cvt_pk_bf16_f32 v7, v18, v20
	v_add_co_u32_e32 v8, vcc, s41, v40
	global_store_dwordx4 v[40:41], v[4:7], off
	s_mov_b32 s77, 0x8000
	s_mov_b32 s80, 0x10000
	v_cvt_pk_bf16_f32 v4, v23, v9
	v_cvt_pk_bf16_f32 v5, v11, v13
	v_cvt_pk_bf16_f32 v6, v15, v17
	v_cvt_pk_bf16_f32 v7, v19, v21
	v_addc_co_u32_e32 v9, vcc, 0, v41, vcc
	global_store_dwordx4 v[8:9], v[4:7], off
	v_add_co_u32_e32 v8, vcc, s43, v40
	s_waitcnt lgkmcnt(6)
	v_cvt_pk_bf16_f32 v4, v24, v26
	s_waitcnt lgkmcnt(4)
	v_cvt_pk_bf16_f32 v5, v28, v30
	s_waitcnt lgkmcnt(2)
	v_cvt_pk_bf16_f32 v6, v32, v34
	s_waitcnt lgkmcnt(0)
	v_cvt_pk_bf16_f32 v7, v36, v38
	v_addc_co_u32_e32 v9, vcc, 0, v41, vcc
	global_store_dwordx4 v[8:9], v[4:7], off
	v_add_co_u32_e32 v48, vcc, s42, v40
	s_nop 0
	v_cvt_pk_bf16_f32 v4, v25, v27
	v_cvt_pk_bf16_f32 v5, v29, v31
	v_cvt_pk_bf16_f32 v6, v33, v35
	v_cvt_pk_bf16_f32 v7, v37, v39
	ds_read2_b32 v[8:9], v165 offset0:97 offset1:105
	ds_read2_b32 v[10:11], v165 offset0:162 offset1:170
	ds_read2_b32 v[12:13], v165 offset0:227 offset1:235
	ds_read2_b32 v[14:15], v49 offset0:36 offset1:44
	ds_read2_b32 v[16:17], v49 offset0:101 offset1:109
	ds_read2_b32 v[18:19], v49 offset0:166 offset1:174
	ds_read2_b32 v[20:21], v49 offset0:231 offset1:239
	ds_read2_b32 v[22:23], v165 offset0:32 offset1:40
	ds_read2_b32 v[24:25], v165 offset0:48 offset1:56
	ds_read2_b32 v[26:27], v165 offset0:113 offset1:121
	ds_read2_b32 v[28:29], v165 offset0:178 offset1:186
	ds_read2_b32 v[30:31], v165 offset0:243 offset1:251
	ds_read2_b32 v[32:33], v49 offset0:52 offset1:60
	ds_read2_b32 v[34:35], v49 offset0:117 offset1:125
	ds_read2_b32 v[36:37], v49 offset0:182 offset1:190
	ds_read2_b32 v[38:39], v49 offset0:247 offset1:255
	s_mov_b32 s83, 0x18000
	v_addc_co_u32_e32 v49, vcc, 0, v41, vcc
	global_store_dwordx4 v[48:49], v[4:7], off
	v_add_co_u32_e32 v48, vcc, s40, v40
	s_waitcnt lgkmcnt(8)
	v_cvt_pk_bf16_f32 v4, v22, v8
	v_addc_co_u32_e32 v49, vcc, 0, v41, vcc
	v_cvt_pk_bf16_f32 v5, v10, v12
	v_cvt_pk_bf16_f32 v6, v14, v16
	v_cvt_pk_bf16_f32 v7, v18, v20
	v_add_co_u32_e32 v8, vcc, s44, v40
	global_store_dwordx4 v[48:49], v[4:7], off
	s_nop 1
	v_cvt_pk_bf16_f32 v4, v23, v9
	v_cvt_pk_bf16_f32 v5, v11, v13
	v_cvt_pk_bf16_f32 v6, v15, v17
	v_cvt_pk_bf16_f32 v7, v19, v21
	v_addc_co_u32_e32 v9, vcc, 0, v41, vcc
	global_store_dwordx4 v[8:9], v[4:7], off
	v_add_co_u32_e32 v8, vcc, s45, v40
	s_waitcnt lgkmcnt(6)
	v_cvt_pk_bf16_f32 v4, v24, v26
	s_waitcnt lgkmcnt(4)
	v_cvt_pk_bf16_f32 v5, v28, v30
	s_waitcnt lgkmcnt(2)
	v_cvt_pk_bf16_f32 v6, v32, v34
	s_waitcnt lgkmcnt(0)
	v_cvt_pk_bf16_f32 v7, v36, v38
	v_addc_co_u32_e32 v9, vcc, 0, v41, vcc
	global_store_dwordx4 v[8:9], v[4:7], off
	v_add_co_u32_e32 v8, vcc, 0x38000, v40
	s_nop 0
	v_cvt_pk_bf16_f32 v4, v25, v27
	v_cvt_pk_bf16_f32 v5, v29, v31
	v_cvt_pk_bf16_f32 v6, v33, v35
	v_cvt_pk_bf16_f32 v7, v37, v39
	v_addc_co_u32_e32 v9, vcc, 0, v41, vcc
	global_store_dwordx4 v[8:9], v[4:7], off
.LBB0_90:
	s_andn2_saveexec_b64 s[50:51], s[50:51]
	s_cbranch_execz .LBB0_92
	v_add_u32_e32 v47, 0xfffff6b0, v46
	v_mov_b32_e32 v4, s67
	v_mov_b32_e32 v5, s65
	v_cmp_gt_u32_e32 vcc, s76, v47
	v_mov_b32_e32 v6, s64
	v_readlane_b32 s40, v255, 30
	v_cndmask_b32_e32 v5, v4, v5, vcc
	v_mov_b32_e32 v4, s66
	v_cndmask_b32_e32 v4, v4, v6, vcc
	v_and_b32_e32 v130, 0x7800000, v44
	v_and_b32_e32 v76, 0x3c0, v3
	v_readlane_b32 s41, v255, 31
	v_lshl_add_u64 v[4:5], v[4:5], 0, s[16:17]
	v_add_u32_e32 v77, 0xffffdac0, v42
	v_lshl_add_u64 v[40:41], s[40:41], 0, v[130:131]
	s_movk_i32 s40, 0x7c0
	v_or_b32_e32 v7, v76, v123
	v_lshl_add_u64 v[4:5], v[4:5], 0, v[130:131]
	v_and_or_b32 v6, v77, s40, v162
	v_lshlrev_b32_e32 v130, 13, v7
	v_lshl_add_u64 v[4:5], v[4:5], 0, v[130:131]
	v_lshlrev_b32_e32 v130, 2, v6
	v_lshl_add_u64 v[68:69], v[4:5], 0, v[130:131]
	s_mov_b32 s41, 0x8000
	s_waitcnt lgkmcnt(0)
	v_add_co_u32_e32 v8, vcc, s41, v68
	s_mov_b32 s43, 0x10000
	s_nop 0
	v_addc_co_u32_e32 v9, vcc, 0, v69, vcc
	v_add_co_u32_e32 v12, vcc, s43, v68
	s_mov_b32 s42, 0x18000
	s_nop 0
	v_addc_co_u32_e32 v13, vcc, 0, v69, vcc
	v_add_co_u32_e32 v16, vcc, s42, v68
	s_mov_b32 s40, 0x20000
	s_nop 0
	v_addc_co_u32_e32 v17, vcc, 0, v69, vcc
	v_add_co_u32_e32 v20, vcc, s40, v68
	s_mov_b32 s40, 0x28000
	s_nop 0
	v_addc_co_u32_e32 v21, vcc, 0, v69, vcc
	v_add_co_u32_e32 v24, vcc, s40, v68
	s_mov_b32 s40, 0x30000
	s_nop 0
	v_addc_co_u32_e32 v25, vcc, 0, v69, vcc
	v_add_co_u32_e32 v28, vcc, s40, v68
	s_mov_b32 s40, 0x38000
	s_nop 0
	v_addc_co_u32_e32 v29, vcc, 0, v69, vcc
	v_add_co_u32_e32 v32, vcc, s40, v68
	s_mov_b32 s40, 0x40000
	s_nop 0
	v_addc_co_u32_e32 v33, vcc, 0, v69, vcc
	v_add_co_u32_e32 v36, vcc, s40, v68
	s_mov_b32 s40, 0x48000
	s_nop 0
	v_addc_co_u32_e32 v37, vcc, 0, v69, vcc
	v_add_co_u32_e32 v48, vcc, s40, v68
	s_mov_b32 s40, 0x50000
	s_nop 0
	v_addc_co_u32_e32 v49, vcc, 0, v69, vcc
	v_add_co_u32_e32 v52, vcc, s40, v68
	s_mov_b32 s40, 0x58000
	s_nop 0
	v_addc_co_u32_e32 v53, vcc, 0, v69, vcc
	v_add_co_u32_e32 v56, vcc, s40, v68
	s_mov_b32 s40, 0x60000
	s_nop 0
	v_addc_co_u32_e32 v57, vcc, 0, v69, vcc
	v_add_co_u32_e32 v60, vcc, s40, v68
	s_mov_b32 s40, 0x68000
	s_nop 0
	v_addc_co_u32_e32 v61, vcc, 0, v69, vcc
	v_add_co_u32_e32 v64, vcc, s40, v68
	s_mov_b32 s40, 0x70000
	s_nop 0
	v_addc_co_u32_e32 v65, vcc, 0, v69, vcc
	v_add_co_u32_e32 v70, vcc, s40, v68
	s_mov_b32 s40, 0x78000
	s_nop 0
	v_addc_co_u32_e32 v71, vcc, 0, v69, vcc
	v_add_co_u32_e32 v72, vcc, s40, v68
	global_load_dwordx4 v[4:7], v[68:69], off nt
	s_nop 0
	global_load_dwordx4 v[8:11], v[8:9], off nt
	v_addc_co_u32_e32 v73, vcc, 0, v69, vcc
	global_load_dwordx4 v[12:15], v[12:13], off nt
	s_nop 0
	global_load_dwordx4 v[16:19], v[16:17], off nt
	s_nop 0
	global_load_dwordx4 v[20:23], v[20:21], off nt
	s_nop 0
	global_load_dwordx4 v[24:27], v[24:25], off nt
	s_nop 0
	global_load_dwordx4 v[28:31], v[28:29], off nt
	s_nop 0
	global_load_dwordx4 v[32:35], v[32:33], off nt
	s_nop 0
	global_load_dwordx4 v[36:39], v[36:37], off nt
	s_nop 0
	global_load_dwordx4 v[48:51], v[48:49], off nt
	s_nop 0
	global_load_dwordx4 v[52:55], v[52:53], off nt
	s_nop 0
	global_load_dwordx4 v[56:59], v[56:57], off nt
	s_nop 0
	global_load_dwordx4 v[60:63], v[60:61], off nt
	s_nop 0
	global_load_dwordx4 v[64:67], v[64:65], off nt
	s_nop 0
	global_load_dwordx4 v[68:71], v[70:71], off nt
	s_nop 0
	global_load_dwordx4 v[72:75], v[72:73], off nt
	s_waitcnt vmcnt(0)
	ds_write2_b32 v163, v4, v5 offset1:1
	ds_write2_b32 v163, v6, v7 offset0:2 offset1:3
	v_add_u32_e32 v4, 0x410, v163
	ds_write2_b32 v4, v8, v9 offset1:1
	v_add_u32_e32 v4, 0x418, v163
	ds_write2_b32 v4, v10, v11 offset1:1
	v_add_u32_e32 v4, 0x820, v163
	ds_write2_b32 v4, v12, v13 offset1:1
	v_add_u32_e32 v4, 0x828, v163
	ds_write2_b32 v4, v14, v15 offset1:1
	v_add_u32_e32 v4, 0xc30, v163
	ds_write2_b32 v4, v16, v17 offset1:1
	v_add_u32_e32 v4, 0xc38, v163
	ds_write2_b32 v4, v18, v19 offset1:1
	v_add_u32_e32 v4, 0x1040, v163
	ds_write2_b32 v4, v20, v21 offset1:1
	v_add_u32_e32 v4, 0x1048, v163
	ds_write2_b32 v4, v22, v23 offset1:1
	v_add_u32_e32 v4, 0x1450, v163
	ds_write2_b32 v4, v24, v25 offset1:1
	v_add_u32_e32 v4, 0x1458, v163
	ds_write2_b32 v4, v26, v27 offset1:1
	v_add_u32_e32 v4, 0x1860, v163
	ds_write2_b32 v4, v28, v29 offset1:1
	v_add_u32_e32 v4, 0x1868, v163
	ds_write2_b32 v4, v30, v31 offset1:1
	v_add_u32_e32 v4, 0x1c70, v163
	ds_write2_b32 v4, v32, v33 offset1:1
	v_add_u32_e32 v4, 0x1c78, v163
	ds_write2_b32 v4, v34, v35 offset1:1
	v_add_u32_e32 v4, 0x2080, v163
	ds_write2_b32 v4, v36, v37 offset1:1
	v_add_u32_e32 v4, 0x2088, v163
	ds_write2_b32 v4, v38, v39 offset1:1
	v_add_u32_e32 v4, 0x2490, v163
	ds_write2_b32 v4, v48, v49 offset1:1
	v_add_u32_e32 v4, 0x2498, v163
	ds_write2_b32 v4, v50, v51 offset1:1
	v_add_u32_e32 v4, 0x28a0, v163
	ds_write2_b32 v4, v52, v53 offset1:1
	v_add_u32_e32 v4, 0x28a8, v163
	ds_write2_b32 v4, v54, v55 offset1:1
	v_add_u32_e32 v4, 0x2cb0, v163
	ds_write2_b32 v4, v56, v57 offset1:1
	v_add_u32_e32 v4, 0x2cb8, v163
	ds_write2_b32 v4, v58, v59 offset1:1
	v_add_u32_e32 v4, 0x30c0, v163
	ds_write2_b32 v4, v60, v61 offset1:1
	v_add_u32_e32 v4, 0x30c8, v163
	ds_write2_b32 v4, v62, v63 offset1:1
	v_add_u32_e32 v4, 0x34d0, v163
	ds_write2_b32 v4, v64, v65 offset1:1
	v_add_u32_e32 v4, 0x34d8, v163
	ds_write2_b32 v4, v66, v67 offset1:1
	v_add_u32_e32 v4, 0x38e0, v163
	ds_write2_b32 v4, v68, v69 offset1:1
	v_add_u32_e32 v4, 0x38e8, v163
	ds_write2_b32 v4, v70, v71 offset1:1
	v_add_u32_e32 v4, 0x3cf0, v163
	ds_write2_b32 v4, v72, v73 offset1:1
	v_add_u32_e32 v4, 0x3cf8, v163
	s_movk_i32 s40, 0x1fff
	ds_write2_b32 v4, v74, v75 offset1:1
	v_cmp_lt_u32_e32 vcc, s40, v47
	v_add_u32_e32 v47, 0x400, v165
	ds_read2_b32 v[8:9], v165 offset0:65 offset1:73
	ds_read2_b32 v[10:11], v165 offset0:130 offset1:138
	ds_read2_b32 v[12:13], v165 offset0:195 offset1:203
	ds_read2_b32 v[14:15], v47 offset0:4 offset1:12
	ds_read2_b32 v[16:17], v47 offset0:69 offset1:77
	ds_read2_b32 v[18:19], v47 offset0:134 offset1:142
	ds_read2_b32 v[20:21], v47 offset0:199 offset1:207
	ds_read2_b32 v[22:23], v165 offset1:8
	ds_read2_b32 v[24:25], v165 offset0:16 offset1:24
	ds_read2_b32 v[26:27], v165 offset0:81 offset1:89
	ds_read2_b32 v[28:29], v165 offset0:146 offset1:154
	ds_read2_b32 v[30:31], v165 offset0:211 offset1:219
	ds_read2_b32 v[32:33], v47 offset0:20 offset1:28
	ds_read2_b32 v[34:35], v47 offset0:85 offset1:93
	ds_read2_b32 v[36:37], v47 offset0:150 offset1:158
	ds_read2_b32 v[38:39], v47 offset0:215 offset1:223
	v_lshlrev_b32_e32 v130, 1, v76
	v_lshl_add_u64 v[4:5], v[40:41], 0, v[130:131]
	v_lshlrev_b32_e32 v130, 1, v116
	v_cndmask_b32_e32 v6, 0, v229, vcc
	v_lshl_add_u64 v[40:41], v[4:5], 0, v[130:131]
	v_lshlrev_b32_e32 v4, 1, v77
	v_and_b32_e32 v4, 0xf00, v4
	v_and_or_b32 v5, v77, 64, v6
	v_or3_b32 v48, v5, v4, v164
	v_lshlrev_b32_e32 v130, 11, v48
	v_lshl_add_u64 v[40:41], v[40:41], 0, v[130:131]
	s_waitcnt lgkmcnt(8)
	v_cvt_pk_bf16_f32 v4, v22, v8
	v_cvt_pk_bf16_f32 v5, v10, v12
	v_cvt_pk_bf16_f32 v6, v14, v16
	v_cvt_pk_bf16_f32 v7, v18, v20
	v_add_co_u32_e32 v8, vcc, s88, v40
	global_store_dwordx4 v[40:41], v[4:7], off
	s_mov_b32 s77, 0x8000
	s_nop 0
	v_cvt_pk_bf16_f32 v4, v23, v9
	v_cvt_pk_bf16_f32 v5, v11, v13
	v_cvt_pk_bf16_f32 v6, v15, v17
	v_cvt_pk_bf16_f32 v7, v19, v21
	v_addc_co_u32_e32 v9, vcc, 0, v41, vcc
	global_store_dwordx4 v[8:9], v[4:7], off
	v_add_co_u32_e32 v8, vcc, s41, v40
	s_waitcnt lgkmcnt(6)
	v_cvt_pk_bf16_f32 v4, v24, v26
	s_waitcnt lgkmcnt(4)
	v_cvt_pk_bf16_f32 v5, v28, v30
	s_waitcnt lgkmcnt(2)
	v_cvt_pk_bf16_f32 v6, v32, v34
	s_waitcnt lgkmcnt(0)
	v_cvt_pk_bf16_f32 v7, v36, v38
	v_addc_co_u32_e32 v9, vcc, 0, v41, vcc
	global_store_dwordx4 v[8:9], v[4:7], off
	v_add_co_u32_e32 v48, vcc, s82, v40
	s_nop 0
	v_cvt_pk_bf16_f32 v4, v25, v27
	v_cvt_pk_bf16_f32 v5, v29, v31
	v_cvt_pk_bf16_f32 v6, v33, v35
	v_cvt_pk_bf16_f32 v7, v37, v39
	ds_read2_b32 v[8:9], v165 offset0:97 offset1:105
	ds_read2_b32 v[10:11], v165 offset0:162 offset1:170
	ds_read2_b32 v[12:13], v165 offset0:227 offset1:235
	ds_read2_b32 v[14:15], v47 offset0:36 offset1:44
	ds_read2_b32 v[16:17], v47 offset0:101 offset1:109
	ds_read2_b32 v[18:19], v47 offset0:166 offset1:174
	ds_read2_b32 v[20:21], v47 offset0:231 offset1:239
	ds_read2_b32 v[22:23], v165 offset0:32 offset1:40
	ds_read2_b32 v[24:25], v165 offset0:48 offset1:56
	ds_read2_b32 v[26:27], v165 offset0:113 offset1:121
	ds_read2_b32 v[28:29], v165 offset0:178 offset1:186
	ds_read2_b32 v[30:31], v165 offset0:243 offset1:251
	ds_read2_b32 v[32:33], v47 offset0:52 offset1:60
	ds_read2_b32 v[34:35], v47 offset0:117 offset1:125
	ds_read2_b32 v[36:37], v47 offset0:182 offset1:190
	ds_read2_b32 v[38:39], v47 offset0:247 offset1:255
	v_addc_co_u32_e32 v49, vcc, 0, v41, vcc
	global_store_dwordx4 v[48:49], v[4:7], off
	v_add_co_u32_e32 v48, vcc, s43, v40
	s_mov_b32 s40, 0x14000
	s_nop 0
	v_addc_co_u32_e32 v49, vcc, 0, v41, vcc
	s_waitcnt lgkmcnt(8)
	v_cvt_pk_bf16_f32 v4, v22, v8
	v_cvt_pk_bf16_f32 v5, v10, v12
	v_cvt_pk_bf16_f32 v6, v14, v16
	v_cvt_pk_bf16_f32 v7, v18, v20
	v_add_co_u32_e32 v8, vcc, s40, v40
	global_store_dwordx4 v[48:49], v[4:7], off
	s_mov_b32 s80, 0x10000
	s_mov_b32 s83, 0x18000
	v_cvt_pk_bf16_f32 v4, v23, v9
	v_cvt_pk_bf16_f32 v5, v11, v13
	v_cvt_pk_bf16_f32 v6, v15, v17
	v_cvt_pk_bf16_f32 v7, v19, v21
	v_addc_co_u32_e32 v9, vcc, 0, v41, vcc
	global_store_dwordx4 v[8:9], v[4:7], off
	v_add_co_u32_e32 v8, vcc, s42, v40
	s_waitcnt lgkmcnt(6)
	v_cvt_pk_bf16_f32 v4, v24, v26
	s_waitcnt lgkmcnt(4)
	v_cvt_pk_bf16_f32 v5, v28, v30
	s_waitcnt lgkmcnt(2)
	v_cvt_pk_bf16_f32 v6, v32, v34
	s_waitcnt lgkmcnt(0)
	v_cvt_pk_bf16_f32 v7, v36, v38
	v_addc_co_u32_e32 v9, vcc, 0, v41, vcc
	global_store_dwordx4 v[8:9], v[4:7], off
	v_add_co_u32_e32 v8, vcc, 0x1c000, v40
	s_nop 0
	v_cvt_pk_bf16_f32 v4, v25, v27
	v_cvt_pk_bf16_f32 v5, v29, v31
	v_cvt_pk_bf16_f32 v6, v33, v35
	v_cvt_pk_bf16_f32 v7, v37, v39
	v_addc_co_u32_e32 v9, vcc, 0, v41, vcc
	global_store_dwordx4 v[8:9], v[4:7], off

.LBB0_93:
	s_andn2_saveexec_b64 s[48:49], s[48:49]
	s_cbranch_execz .LBB0_95
	v_and_b32_e32 v47, 0x3c0, v3
	v_and_b32_e32 v4, 0x3fc0, v42
	v_or_b32_e32 v5, v47, v123
	v_add_u32_e32 v76, 0xffffdec0, v4
	v_lshlrev_b32_e32 v130, 12, v5
	v_or_b32_e32 v4, v76, v162
	v_lshl_add_u64 v[6:7], s[20:21], 0, v[130:131]
	v_mov_b32_e32 v5, v131
	v_lshl_add_u64 v[40:41], v[4:5], 2, v[6:7]
	s_waitcnt lgkmcnt(0)
	v_add_co_u32_e32 v8, vcc, 0x4000, v40
	s_mov_b32 s40, 0x20000
	s_nop 0
	v_addc_co_u32_e32 v9, vcc, 0, v41, vcc
	v_add_co_u32_e32 v12, vcc, 0x8000, v40
	global_load_dwordx4 v[4:7], v[40:41], off nt
	s_nop 0
	global_load_dwordx4 v[8:11], v[8:9], off nt
	v_addc_co_u32_e32 v13, vcc, 0, v41, vcc
	v_add_co_u32_e32 v16, vcc, 0xc000, v40
	s_nop 1
	v_addc_co_u32_e32 v17, vcc, 0, v41, vcc
	v_add_co_u32_e32 v20, vcc, 0x10000, v40
	global_load_dwordx4 v[12:15], v[12:13], off nt
	s_nop 0
	global_load_dwordx4 v[16:19], v[16:17], off nt
	v_addc_co_u32_e32 v21, vcc, 0, v41, vcc
	v_add_co_u32_e32 v24, vcc, 0x14000, v40
	s_nop 1
	v_addc_co_u32_e32 v25, vcc, 0, v41, vcc
	v_add_co_u32_e32 v28, vcc, 0x18000, v40
	global_load_dwordx4 v[20:23], v[20:21], off nt
	s_nop 0
	global_load_dwordx4 v[24:27], v[24:25], off nt
	v_addc_co_u32_e32 v29, vcc, 0, v41, vcc
	v_add_co_u32_e32 v32, vcc, 0x1c000, v40
	s_nop 1
	v_addc_co_u32_e32 v33, vcc, 0, v41, vcc
	v_add_co_u32_e32 v36, vcc, s40, v40
	global_load_dwordx4 v[28:31], v[28:29], off nt
	s_nop 0
	global_load_dwordx4 v[32:35], v[32:33], off nt
	v_addc_co_u32_e32 v37, vcc, 0, v41, vcc
	v_add_co_u32_e32 v48, vcc, 0x24000, v40
	s_nop 1
	v_addc_co_u32_e32 v49, vcc, 0, v41, vcc
	v_add_co_u32_e32 v52, vcc, 0x28000, v40
	global_load_dwordx4 v[36:39], v[36:37], off nt
	s_nop 0
	global_load_dwordx4 v[48:51], v[48:49], off nt
	v_addc_co_u32_e32 v53, vcc, 0, v41, vcc
	v_add_co_u32_e32 v56, vcc, 0x2c000, v40
	s_nop 1
	v_addc_co_u32_e32 v57, vcc, 0, v41, vcc
	v_add_co_u32_e32 v60, vcc, 0x30000, v40
	global_load_dwordx4 v[52:55], v[52:53], off nt
	s_nop 0
	global_load_dwordx4 v[56:59], v[56:57], off nt
	v_addc_co_u32_e32 v61, vcc, 0, v41, vcc
	v_add_co_u32_e32 v64, vcc, 0x34000, v40
	s_nop 1
	v_addc_co_u32_e32 v65, vcc, 0, v41, vcc
	v_add_co_u32_e32 v68, vcc, 0x38000, v40
	global_load_dwordx4 v[60:63], v[60:61], off nt
	s_nop 0
	global_load_dwordx4 v[64:67], v[64:65], off nt
	v_addc_co_u32_e32 v69, vcc, 0, v41, vcc
	v_add_co_u32_e32 v40, vcc, 0x3c000, v40
	s_nop 1
	v_addc_co_u32_e32 v41, vcc, 0, v41, vcc
	global_load_dwordx4 v[68:71], v[68:69], off nt
	s_nop 0
	global_load_dwordx4 v[72:75], v[40:41], off nt
	s_waitcnt vmcnt(0)
	ds_write2_b32 v163, v4, v5 offset1:1
	ds_write2_b32 v163, v6, v7 offset0:2 offset1:3
	v_add_u32_e32 v4, 0x410, v163
	ds_write2_b32 v4, v8, v9 offset1:1
	v_add_u32_e32 v4, 0x418, v163
	ds_write2_b32 v4, v10, v11 offset1:1
	v_add_u32_e32 v4, 0x820, v163
	ds_write2_b32 v4, v12, v13 offset1:1
	v_add_u32_e32 v4, 0x828, v163
	ds_write2_b32 v4, v14, v15 offset1:1
	v_add_u32_e32 v4, 0xc30, v163
	ds_write2_b32 v4, v16, v17 offset1:1
	v_add_u32_e32 v4, 0xc38, v163
	ds_write2_b32 v4, v18, v19 offset1:1
	v_add_u32_e32 v4, 0x1040, v163
	ds_write2_b32 v4, v20, v21 offset1:1
	v_add_u32_e32 v4, 0x1048, v163
	ds_write2_b32 v4, v22, v23 offset1:1
	v_add_u32_e32 v4, 0x1450, v163
	ds_write2_b32 v4, v24, v25 offset1:1
	v_add_u32_e32 v4, 0x1458, v163
	ds_write2_b32 v4, v26, v27 offset1:1
	v_add_u32_e32 v4, 0x1860, v163
	ds_write2_b32 v4, v28, v29 offset1:1
	v_add_u32_e32 v4, 0x1868, v163
	ds_write2_b32 v4, v30, v31 offset1:1
	v_add_u32_e32 v4, 0x1c70, v163
	ds_write2_b32 v4, v32, v33 offset1:1
	v_add_u32_e32 v4, 0x1c78, v163
	ds_write2_b32 v4, v34, v35 offset1:1
	v_add_u32_e32 v4, 0x2080, v163
	ds_write2_b32 v4, v36, v37 offset1:1
	v_add_u32_e32 v4, 0x2088, v163
	ds_write2_b32 v4, v38, v39 offset1:1
	v_add_u32_e32 v4, 0x2490, v163
	ds_write2_b32 v4, v48, v49 offset1:1
	v_add_u32_e32 v4, 0x2498, v163
	ds_write2_b32 v4, v50, v51 offset1:1
	v_add_u32_e32 v4, 0x28a0, v163
	ds_write2_b32 v4, v52, v53 offset1:1
	v_add_u32_e32 v4, 0x28a8, v163
	ds_write2_b32 v4, v54, v55 offset1:1
	v_add_u32_e32 v4, 0x2cb0, v163
	ds_write2_b32 v4, v56, v57 offset1:1
	v_add_u32_e32 v4, 0x2cb8, v163
	ds_write2_b32 v4, v58, v59 offset1:1
	v_add_u32_e32 v4, 0x30c0, v163
	ds_write2_b32 v4, v60, v61 offset1:1
	v_add_u32_e32 v4, 0x30c8, v163
	ds_write2_b32 v4, v62, v63 offset1:1
	v_add_u32_e32 v4, 0x34d0, v163
	ds_write2_b32 v4, v64, v65 offset1:1
	v_add_u32_e32 v4, 0x34d8, v163
	ds_write2_b32 v4, v66, v67 offset1:1
	v_add_u32_e32 v4, 0x38e0, v163
	ds_write2_b32 v4, v68, v69 offset1:1
	v_add_u32_e32 v4, 0x38e8, v163
	ds_write2_b32 v4, v70, v71 offset1:1
	v_add_u32_e32 v4, 0x3cf0, v163
	ds_write2_b32 v4, v72, v73 offset1:1
	v_add_u32_e32 v4, 0x3cf8, v163
	ds_write2_b32 v4, v74, v75 offset1:1
	v_add_u32_e32 v48, 0x400, v165
	ds_read2_b32 v[8:9], v165 offset0:65 offset1:73
	ds_read2_b32 v[10:11], v165 offset0:130 offset1:138
	ds_read2_b32 v[12:13], v165 offset0:195 offset1:203
	ds_read2_b32 v[14:15], v48 offset0:4 offset1:12
	ds_read2_b32 v[16:17], v48 offset0:69 offset1:77
	ds_read2_b32 v[18:19], v48 offset0:134 offset1:142
	ds_read2_b32 v[20:21], v48 offset0:199 offset1:207
	ds_read2_b32 v[22:23], v165 offset1:8
	ds_read2_b32 v[24:25], v165 offset0:16 offset1:24
	ds_read2_b32 v[26:27], v165 offset0:81 offset1:89
	ds_read2_b32 v[28:29], v165 offset0:146 offset1:154
	ds_read2_b32 v[30:31], v165 offset0:211 offset1:219
	ds_read2_b32 v[32:33], v48 offset0:20 offset1:28
	ds_read2_b32 v[34:35], v48 offset0:85 offset1:93
	ds_read2_b32 v[36:37], v48 offset0:150 offset1:158
	ds_read2_b32 v[38:39], v48 offset0:215 offset1:223
	v_lshlrev_b32_e32 v130, 1, v47
	v_or_b32_e32 v49, v76, v164
	v_lshl_add_u64 v[40:41], v[118:119], 0, v[130:131]
	v_lshlrev_b32_e32 v130, 11, v49
	v_lshl_add_u64 v[40:41], v[40:41], 0, v[130:131]
	s_waitcnt lgkmcnt(8)
	v_cvt_pk_bf16_f32 v4, v22, v8
	v_cvt_pk_bf16_f32 v5, v10, v12
	v_cvt_pk_bf16_f32 v6, v14, v16
	v_cvt_pk_bf16_f32 v7, v18, v20
	v_add_co_u32_e32 v8, vcc, s88, v40
	global_store_dwordx4 v[40:41], v[4:7], off
	s_nop 1
	v_cvt_pk_bf16_f32 v4, v23, v9
	v_cvt_pk_bf16_f32 v5, v11, v13
	v_cvt_pk_bf16_f32 v6, v15, v17
	v_cvt_pk_bf16_f32 v7, v19, v21
	v_addc_co_u32_e32 v9, vcc, 0, v41, vcc
	global_store_dwordx4 v[8:9], v[4:7], off
	v_add_co_u32_e32 v8, vcc, s77, v40
	s_waitcnt lgkmcnt(6)
	v_cvt_pk_bf16_f32 v4, v24, v26
	s_waitcnt lgkmcnt(4)
	v_cvt_pk_bf16_f32 v5, v28, v30
	s_waitcnt lgkmcnt(2)
	v_cvt_pk_bf16_f32 v6, v32, v34
	s_waitcnt lgkmcnt(0)
	v_cvt_pk_bf16_f32 v7, v36, v38
	v_addc_co_u32_e32 v9, vcc, 0, v41, vcc
	global_store_dwordx4 v[8:9], v[4:7], off
	s_nop 1
	v_cvt_pk_bf16_f32 v4, v25, v27
	v_cvt_pk_bf16_f32 v5, v29, v31
	v_cvt_pk_bf16_f32 v6, v33, v35
	v_cvt_pk_bf16_f32 v7, v37, v39
	ds_read2_b32 v[8:9], v165 offset0:97 offset1:105
	ds_read2_b32 v[10:11], v165 offset0:162 offset1:170
	ds_read2_b32 v[12:13], v165 offset0:227 offset1:235
	ds_read2_b32 v[14:15], v48 offset0:36 offset1:44
	ds_read2_b32 v[16:17], v48 offset0:101 offset1:109
	ds_read2_b32 v[18:19], v48 offset0:166 offset1:174
	ds_read2_b32 v[20:21], v48 offset0:231 offset1:239
	ds_read2_b32 v[22:23], v165 offset0:32 offset1:40
	ds_read2_b32 v[24:25], v165 offset0:48 offset1:56
	ds_read2_b32 v[26:27], v165 offset0:113 offset1:121
	ds_read2_b32 v[28:29], v165 offset0:178 offset1:186
	ds_read2_b32 v[30:31], v165 offset0:243 offset1:251
	ds_read2_b32 v[32:33], v48 offset0:52 offset1:60
	ds_read2_b32 v[34:35], v48 offset0:117 offset1:125
	ds_read2_b32 v[36:37], v48 offset0:182 offset1:190
	ds_read2_b32 v[38:39], v48 offset0:247 offset1:255
	v_add_co_u32_e32 v48, vcc, s82, v40
	s_nop 1
	v_addc_co_u32_e32 v49, vcc, 0, v41, vcc
	global_store_dwordx4 v[48:49], v[4:7], off
	v_add_co_u32_e32 v48, vcc, s80, v40
	s_mov_b32 s40, 0x14000
	s_nop 0
	v_addc_co_u32_e32 v49, vcc, 0, v41, vcc
	s_waitcnt lgkmcnt(8)
	v_cvt_pk_bf16_f32 v4, v22, v8
	v_cvt_pk_bf16_f32 v5, v10, v12
	v_cvt_pk_bf16_f32 v6, v14, v16
	v_cvt_pk_bf16_f32 v7, v18, v20
	v_add_co_u32_e32 v8, vcc, s40, v40
	global_store_dwordx4 v[48:49], v[4:7], off
	s_nop 1
	v_cvt_pk_bf16_f32 v4, v23, v9
	v_cvt_pk_bf16_f32 v5, v11, v13
	v_cvt_pk_bf16_f32 v6, v15, v17
	v_cvt_pk_bf16_f32 v7, v19, v21
	v_addc_co_u32_e32 v9, vcc, 0, v41, vcc
	global_store_dwordx4 v[8:9], v[4:7], off
	v_add_co_u32_e32 v8, vcc, s83, v40
	s_waitcnt lgkmcnt(6)
	v_cvt_pk_bf16_f32 v4, v24, v26
	s_waitcnt lgkmcnt(4)
	v_cvt_pk_bf16_f32 v5, v28, v30
	s_waitcnt lgkmcnt(2)
	v_cvt_pk_bf16_f32 v6, v32, v34
	s_waitcnt lgkmcnt(0)
	v_cvt_pk_bf16_f32 v7, v36, v38
	v_addc_co_u32_e32 v9, vcc, 0, v41, vcc
	global_store_dwordx4 v[8:9], v[4:7], off
	v_add_co_u32_e32 v8, vcc, 0x1c000, v40
	s_nop 0
	v_cvt_pk_bf16_f32 v4, v25, v27
	v_cvt_pk_bf16_f32 v5, v29, v31
	v_cvt_pk_bf16_f32 v6, v33, v35
	v_cvt_pk_bf16_f32 v7, v37, v39
	v_addc_co_u32_e32 v9, vcc, 0, v41, vcc
	global_store_dwordx4 v[8:9], v[4:7], off

.LBB0_96:
	s_andn2_saveexec_b64 s[46:47], s[46:47]
	s_cbranch_execz .LBB0_98
	v_add_u32_e32 v4, 0xfffff930, v46
	v_lshrrev_b32_e32 v130, 7, v4
	v_lshl_add_u64 v[4:5], s[24:25], 0, v[130:131]
	v_readlane_b32 s48, v251, 35
	v_and_b32_e32 v47, 0x1c0, v3
	v_lshlrev_b64 v[4:5], 21, v[4:5]
	v_readlane_b32 s58, v251, 45
	v_readlane_b32 s59, v251, 46
	v_and_b32_e32 v76, 0x3c0, v43
	v_or_b32_e32 v7, v47, v123
	v_lshl_add_u64 v[4:5], s[58:59], 0, v[4:5]
	v_lshlrev_b64 v[40:41], 20, v[130:131]
	v_or_b32_e32 v6, v76, v162
	v_lshlrev_b32_e32 v130, 12, v7
	v_lshl_add_u64 v[4:5], v[4:5], 0, v[130:131]
	v_lshlrev_b32_e32 v130, 2, v6
	v_lshl_add_u64 v[68:69], v[4:5], 0, v[130:131]
	s_waitcnt lgkmcnt(0)
	v_add_co_u32_e32 v8, vcc, s88, v68
	s_mov_b32 s41, 0x8000
	s_nop 0
	v_addc_co_u32_e32 v9, vcc, 0, v69, vcc
	v_add_co_u32_e32 v12, vcc, s41, v68
	s_mov_b32 s42, 0xc000
	s_nop 0
	v_addc_co_u32_e32 v13, vcc, 0, v69, vcc
	v_add_co_u32_e32 v16, vcc, s42, v68
	s_mov_b32 s40, 0x14000
	s_nop 0
	v_addc_co_u32_e32 v17, vcc, 0, v69, vcc
	v_add_co_u32_e32 v20, vcc, s80, v68
	global_load_dwordx4 v[4:7], v[68:69], off nt
	s_nop 0
	global_load_dwordx4 v[8:11], v[8:9], off nt
	v_addc_co_u32_e32 v21, vcc, 0, v69, vcc
	v_add_co_u32_e32 v24, vcc, s40, v68
	s_mov_b32 s40, 0x1c000
	s_nop 0
	v_addc_co_u32_e32 v25, vcc, 0, v69, vcc
	v_add_co_u32_e32 v28, vcc, s83, v68
	global_load_dwordx4 v[12:15], v[12:13], off nt
	s_nop 0
	global_load_dwordx4 v[16:19], v[16:17], off nt
	v_addc_co_u32_e32 v29, vcc, 0, v69, vcc
	v_add_co_u32_e32 v32, vcc, s40, v68
	s_mov_b32 s40, 0x20000
	s_nop 0
	v_addc_co_u32_e32 v33, vcc, 0, v69, vcc
	v_add_co_u32_e32 v36, vcc, s40, v68
	s_mov_b32 s40, 0x24000
	s_nop 0
	v_addc_co_u32_e32 v37, vcc, 0, v69, vcc
	v_add_co_u32_e32 v48, vcc, s40, v68
	s_mov_b32 s40, 0x28000
	s_nop 0
	v_addc_co_u32_e32 v49, vcc, 0, v69, vcc
	v_add_co_u32_e32 v52, vcc, s40, v68
	s_mov_b32 s40, 0x2c000
	s_nop 0
	v_addc_co_u32_e32 v53, vcc, 0, v69, vcc
	v_add_co_u32_e32 v56, vcc, s40, v68
	s_mov_b32 s40, 0x30000
	s_nop 0
	v_addc_co_u32_e32 v57, vcc, 0, v69, vcc
	v_add_co_u32_e32 v60, vcc, s40, v68
	s_mov_b32 s40, 0x34000
	s_nop 0
	v_addc_co_u32_e32 v61, vcc, 0, v69, vcc
	v_add_co_u32_e32 v64, vcc, s40, v68
	s_mov_b32 s40, 0x38000
	s_nop 0
	v_addc_co_u32_e32 v65, vcc, 0, v69, vcc
	v_add_co_u32_e32 v70, vcc, s40, v68
	s_mov_b32 s40, 0x3c000
	s_nop 0
	v_addc_co_u32_e32 v71, vcc, 0, v69, vcc
	v_add_co_u32_e32 v72, vcc, s40, v68
	global_load_dwordx4 v[20:23], v[20:21], off nt
	s_nop 0
	global_load_dwordx4 v[24:27], v[24:25], off nt
	v_addc_co_u32_e32 v73, vcc, 0, v69, vcc
	global_load_dwordx4 v[28:31], v[28:29], off nt
	s_nop 0
	global_load_dwordx4 v[32:35], v[32:33], off nt
	s_nop 0
	global_load_dwordx4 v[36:39], v[36:37], off nt
	s_nop 0
	global_load_dwordx4 v[48:51], v[48:49], off nt
	s_nop 0
	global_load_dwordx4 v[52:55], v[52:53], off nt
	s_nop 0
	global_load_dwordx4 v[56:59], v[56:57], off nt
	s_nop 0
	global_load_dwordx4 v[60:63], v[60:61], off nt
	s_nop 0
	global_load_dwordx4 v[64:67], v[64:65], off nt
	s_nop 0
	global_load_dwordx4 v[68:71], v[70:71], off nt
	s_nop 0
	global_load_dwordx4 v[72:75], v[72:73], off nt
	v_readlane_b32 s60, v251, 47
	v_readlane_b32 s61, v251, 48
	v_readlane_b32 s54, v251, 41
	v_readlane_b32 s60, v255, 25
	s_movk_i32 s54, 0x1000
	v_readlane_b32 s61, v255, 26
	v_readlane_b32 s49, v251, 36
	v_readlane_b32 s50, v251, 37
	v_readlane_b32 s51, v251, 38
	v_readlane_b32 s52, v251, 39
	v_readlane_b32 s53, v251, 40
	v_readlane_b32 s55, v251, 42
	v_readlane_b32 s56, v251, 43
	v_readlane_b32 s57, v251, 44
	v_readlane_b32 s62, v251, 49
	v_readlane_b32 s63, v251, 50
	v_lshl_add_u64 v[40:41], s[34:35], 0, v[40:41]
	s_waitcnt vmcnt(0)
	ds_write2_b32 v163, v4, v5 offset1:1
	ds_write2_b32 v163, v6, v7 offset0:2 offset1:3
	v_add_u32_e32 v4, 0x410, v163
	ds_write2_b32 v4, v8, v9 offset1:1
	v_add_u32_e32 v4, 0x418, v163
	ds_write2_b32 v4, v10, v11 offset1:1
	v_add_u32_e32 v4, 0x820, v163
	ds_write2_b32 v4, v12, v13 offset1:1
	v_add_u32_e32 v4, 0x828, v163
	ds_write2_b32 v4, v14, v15 offset1:1
	v_add_u32_e32 v4, 0xc30, v163
	ds_write2_b32 v4, v16, v17 offset1:1
	v_add_u32_e32 v4, 0xc38, v163
	ds_write2_b32 v4, v18, v19 offset1:1
	v_add_u32_e32 v4, 0x1040, v163
	ds_write2_b32 v4, v20, v21 offset1:1
	v_add_u32_e32 v4, 0x1048, v163
	ds_write2_b32 v4, v22, v23 offset1:1
	v_add_u32_e32 v4, 0x1450, v163
	ds_write2_b32 v4, v24, v25 offset1:1
	v_add_u32_e32 v4, 0x1458, v163
	ds_write2_b32 v4, v26, v27 offset1:1
	v_add_u32_e32 v4, 0x1860, v163
	ds_write2_b32 v4, v28, v29 offset1:1
	v_add_u32_e32 v4, 0x1868, v163
	ds_write2_b32 v4, v30, v31 offset1:1
	v_add_u32_e32 v4, 0x1c70, v163
	ds_write2_b32 v4, v32, v33 offset1:1
	v_add_u32_e32 v4, 0x1c78, v163
	ds_write2_b32 v4, v34, v35 offset1:1
	v_add_u32_e32 v4, 0x2080, v163
	ds_write2_b32 v4, v36, v37 offset1:1
	v_add_u32_e32 v4, 0x2088, v163
	ds_write2_b32 v4, v38, v39 offset1:1
	v_add_u32_e32 v4, 0x2490, v163
	ds_write2_b32 v4, v48, v49 offset1:1
	v_add_u32_e32 v4, 0x2498, v163
	ds_write2_b32 v4, v50, v51 offset1:1
	v_add_u32_e32 v4, 0x28a0, v163
	ds_write2_b32 v4, v52, v53 offset1:1
	v_add_u32_e32 v4, 0x28a8, v163
	ds_write2_b32 v4, v54, v55 offset1:1
	v_add_u32_e32 v4, 0x2cb0, v163
	ds_write2_b32 v4, v56, v57 offset1:1
	v_add_u32_e32 v4, 0x2cb8, v163
	ds_write2_b32 v4, v58, v59 offset1:1
	v_add_u32_e32 v4, 0x30c0, v163
	ds_write2_b32 v4, v60, v61 offset1:1
	v_add_u32_e32 v4, 0x30c8, v163
	ds_write2_b32 v4, v62, v63 offset1:1
	v_add_u32_e32 v4, 0x34d0, v163
	ds_write2_b32 v4, v64, v65 offset1:1
	v_add_u32_e32 v4, 0x34d8, v163
	ds_write2_b32 v4, v66, v67 offset1:1
	v_add_u32_e32 v4, 0x38e0, v163
	ds_write2_b32 v4, v68, v69 offset1:1
	v_add_u32_e32 v4, 0x38e8, v163
	ds_write2_b32 v4, v70, v71 offset1:1
	v_add_u32_e32 v4, 0x3cf0, v163
	ds_write2_b32 v4, v72, v73 offset1:1
	v_add_u32_e32 v4, 0x3cf8, v163
	ds_write2_b32 v4, v74, v75 offset1:1
	v_add_u32_e32 v49, 0x400, v165
	ds_read2_b32 v[8:9], v165 offset0:65 offset1:73
	ds_read2_b32 v[10:11], v165 offset0:130 offset1:138
	ds_read2_b32 v[12:13], v165 offset0:195 offset1:203
	ds_read2_b32 v[14:15], v49 offset0:4 offset1:12
	ds_read2_b32 v[16:17], v49 offset0:69 offset1:77
	ds_read2_b32 v[18:19], v49 offset0:134 offset1:142
	ds_read2_b32 v[20:21], v49 offset0:199 offset1:207
	ds_read2_b32 v[22:23], v165 offset1:8
	ds_read2_b32 v[24:25], v165 offset0:16 offset1:24
	ds_read2_b32 v[26:27], v165 offset0:81 offset1:89
	ds_read2_b32 v[28:29], v165 offset0:146 offset1:154
	ds_read2_b32 v[30:31], v165 offset0:211 offset1:219
	ds_read2_b32 v[32:33], v49 offset0:20 offset1:28
	ds_read2_b32 v[34:35], v49 offset0:85 offset1:93
	ds_read2_b32 v[36:37], v49 offset0:150 offset1:158
	ds_read2_b32 v[38:39], v49 offset0:215 offset1:223
	v_lshlrev_b32_e32 v130, 1, v47
	v_lshl_add_u64 v[4:5], v[40:41], 0, v[130:131]
	v_lshlrev_b32_e32 v130, 1, v116
	v_or_b32_e32 v48, v76, v164
	v_lshl_add_u64 v[40:41], v[4:5], 0, v[130:131]
	v_lshlrev_b32_e32 v130, 10, v48
	v_lshl_add_u64 v[40:41], v[40:41], 0, v[130:131]
	s_waitcnt lgkmcnt(8)
	v_cvt_pk_bf16_f32 v4, v22, v8
	v_cvt_pk_bf16_f32 v5, v10, v12
	v_cvt_pk_bf16_f32 v6, v14, v16
	v_cvt_pk_bf16_f32 v7, v18, v20
	v_add_co_u32_e32 v8, vcc, s76, v40
	global_store_dwordx4 v[40:41], v[4:7], off
	s_nop 1
	v_cvt_pk_bf16_f32 v4, v23, v9
	v_cvt_pk_bf16_f32 v5, v11, v13
	v_cvt_pk_bf16_f32 v6, v15, v17
	v_cvt_pk_bf16_f32 v7, v19, v21
	v_addc_co_u32_e32 v9, vcc, 0, v41, vcc
	global_store_dwordx4 v[8:9], v[4:7], off
	v_add_co_u32_e32 v8, vcc, s88, v40
	s_waitcnt lgkmcnt(6)
	v_cvt_pk_bf16_f32 v4, v24, v26
	s_waitcnt lgkmcnt(4)
	v_cvt_pk_bf16_f32 v5, v28, v30
	s_waitcnt lgkmcnt(2)
	v_cvt_pk_bf16_f32 v6, v32, v34
	s_waitcnt lgkmcnt(0)
	v_cvt_pk_bf16_f32 v7, v36, v38
	v_addc_co_u32_e32 v9, vcc, 0, v41, vcc
	global_store_dwordx4 v[8:9], v[4:7], off
	v_add_co_u32_e32 v48, vcc, s75, v40
	s_nop 0
	v_cvt_pk_bf16_f32 v4, v25, v27
	v_cvt_pk_bf16_f32 v5, v29, v31
	v_cvt_pk_bf16_f32 v6, v33, v35
	v_cvt_pk_bf16_f32 v7, v37, v39
	ds_read2_b32 v[8:9], v165 offset0:97 offset1:105
	ds_read2_b32 v[10:11], v165 offset0:162 offset1:170
	ds_read2_b32 v[12:13], v165 offset0:227 offset1:235
	ds_read2_b32 v[14:15], v49 offset0:36 offset1:44
	ds_read2_b32 v[16:17], v49 offset0:101 offset1:109
	ds_read2_b32 v[18:19], v49 offset0:166 offset1:174
	ds_read2_b32 v[20:21], v49 offset0:231 offset1:239
	ds_read2_b32 v[22:23], v165 offset0:32 offset1:40
	ds_read2_b32 v[24:25], v165 offset0:48 offset1:56
	ds_read2_b32 v[26:27], v165 offset0:113 offset1:121
	ds_read2_b32 v[28:29], v165 offset0:178 offset1:186
	ds_read2_b32 v[30:31], v165 offset0:243 offset1:251
	ds_read2_b32 v[32:33], v49 offset0:52 offset1:60
	ds_read2_b32 v[34:35], v49 offset0:117 offset1:125
	ds_read2_b32 v[36:37], v49 offset0:182 offset1:190
	ds_read2_b32 v[38:39], v49 offset0:247 offset1:255
	v_addc_co_u32_e32 v49, vcc, 0, v41, vcc
	global_store_dwordx4 v[48:49], v[4:7], off
	v_add_co_u32_e32 v48, vcc, s41, v40
	s_mov_b32 s40, 0xa000
	s_nop 0
	v_addc_co_u32_e32 v49, vcc, 0, v41, vcc
	s_waitcnt lgkmcnt(8)
	v_cvt_pk_bf16_f32 v4, v22, v8
	v_cvt_pk_bf16_f32 v5, v10, v12
	v_cvt_pk_bf16_f32 v6, v14, v16
	v_cvt_pk_bf16_f32 v7, v18, v20
	v_add_co_u32_e32 v8, vcc, s40, v40
	global_store_dwordx4 v[48:49], v[4:7], off
	s_mov_b32 s77, 0x8000
	s_mov_b32 s82, 0xc000
	v_cvt_pk_bf16_f32 v4, v23, v9
	v_cvt_pk_bf16_f32 v5, v11, v13
	v_cvt_pk_bf16_f32 v6, v15, v17
	v_cvt_pk_bf16_f32 v7, v19, v21
	v_addc_co_u32_e32 v9, vcc, 0, v41, vcc
	global_store_dwordx4 v[8:9], v[4:7], off
	v_add_co_u32_e32 v8, vcc, s42, v40
	s_waitcnt lgkmcnt(6)
	v_cvt_pk_bf16_f32 v4, v24, v26
	s_waitcnt lgkmcnt(4)
	v_cvt_pk_bf16_f32 v5, v28, v30
	s_waitcnt lgkmcnt(2)
	v_cvt_pk_bf16_f32 v6, v32, v34
	s_waitcnt lgkmcnt(0)
	v_cvt_pk_bf16_f32 v7, v36, v38
	v_addc_co_u32_e32 v9, vcc, 0, v41, vcc
	global_store_dwordx4 v[8:9], v[4:7], off
	v_add_co_u32_e32 v8, vcc, 0xe000, v40
	s_nop 0
	v_cvt_pk_bf16_f32 v4, v25, v27
	v_cvt_pk_bf16_f32 v5, v29, v31
	v_cvt_pk_bf16_f32 v6, v33, v35
	v_cvt_pk_bf16_f32 v7, v37, v39
	v_addc_co_u32_e32 v9, vcc, 0, v41, vcc
	global_store_dwordx4 v[8:9], v[4:7], off

.LBB0_99:
	s_andn2_saveexec_b64 s[46:47], s[0:1]
	s_cbranch_execz .LBB0_84
	v_ashrrev_i32_e32 v4, 31, v46
	v_lshrrev_b32_e32 v4, 28, v4
	v_add_u32_e32 v4, v46, v4
	v_ashrrev_i32_e32 v47, 4, v4
	v_lshlrev_b32_e32 v77, 6, v47
	v_or_b32_e32 v6, v77, v162
	s_mov_b32 s0, 0xff93c000
	v_mad_u64_u32 v[4:5], s[0:1], v47, s0, v[2:3]
	v_cmp_gt_i32_e32 vcc, s33, v6
	v_ashrrev_i32_e32 v5, 31, v4
	v_lshl_add_u64 v[4:5], v[4:5], 2, s[22:23]
	v_cndmask_b32_e32 v6, 0, v6, vcc
	v_ashrrev_i32_e32 v7, 31, v6
	v_lshl_add_u64 v[40:41], v[6:7], 2, v[4:5]
	s_mov_b32 s0, 0x1b000
	s_waitcnt lgkmcnt(0)
	v_add_co_u32_e64 v8, s[0:1], s0, v40
	s_nop 1
	v_addc_co_u32_e64 v9, s[0:1], 0, v41, s[0:1]
	s_mov_b32 s0, 0x36000
	s_nop 0
	v_add_co_u32_e64 v12, s[0:1], s0, v40
	global_load_dwordx4 v[4:7], v[40:41], off nt
	s_nop 0
	global_load_dwordx4 v[8:11], v[8:9], off offset:256
	v_addc_co_u32_e64 v13, s[0:1], 0, v41, s[0:1]
	s_mov_b32 s0, 0x51000
	s_nop 0
	v_add_co_u32_e64 v16, s[0:1], s0, v40
	s_nop 1
	v_addc_co_u32_e64 v17, s[0:1], 0, v41, s[0:1]
	s_mov_b32 s0, 0x6c000
	s_nop 0
	v_add_co_u32_e64 v20, s[0:1], s0, v40
	global_load_dwordx4 v[12:15], v[12:13], off offset:512
	s_nop 0
	global_load_dwordx4 v[16:19], v[16:17], off offset:768
	v_addc_co_u32_e64 v21, s[0:1], 0, v41, s[0:1]
	s_mov_b32 s0, 0x87000
	s_nop 0
	v_add_co_u32_e64 v24, s[0:1], s0, v40
	s_nop 1
	v_addc_co_u32_e64 v25, s[0:1], 0, v41, s[0:1]
	s_mov_b32 s0, 0xa2000
	s_nop 0
	v_add_co_u32_e64 v28, s[0:1], s0, v40
	global_load_dwordx4 v[20:23], v[20:21], off offset:1024
	s_nop 0
	global_load_dwordx4 v[24:27], v[24:25], off offset:1280
	v_addc_co_u32_e64 v29, s[0:1], 0, v41, s[0:1]
	s_mov_b32 s0, 0xbd000
	s_nop 0
	v_add_co_u32_e64 v32, s[0:1], s0, v40
	s_nop 1
	v_addc_co_u32_e64 v33, s[0:1], 0, v41, s[0:1]
	s_mov_b32 s0, 0xd8000
	s_nop 0
	v_add_co_u32_e64 v36, s[0:1], s0, v40
	global_load_dwordx4 v[28:31], v[28:29], off offset:1536
	s_nop 0
	global_load_dwordx4 v[32:35], v[32:33], off offset:1792
	v_addc_co_u32_e64 v37, s[0:1], 0, v41, s[0:1]
	s_mov_b32 s0, 0xf3000
	s_nop 0
	v_add_co_u32_e64 v48, s[0:1], s0, v40
	s_nop 1
	v_addc_co_u32_e64 v49, s[0:1], 0, v41, s[0:1]
	s_mov_b32 s0, 0x10e000
	s_nop 0
	v_add_co_u32_e64 v52, s[0:1], s0, v40
	global_load_dwordx4 v[36:39], v[36:37], off offset:2048
	s_nop 0
	global_load_dwordx4 v[48:51], v[48:49], off offset:2304
	v_addc_co_u32_e64 v53, s[0:1], 0, v41, s[0:1]
	s_mov_b32 s0, 0x129000
	s_nop 0
	v_add_co_u32_e64 v56, s[0:1], s0, v40
	s_nop 1
	v_addc_co_u32_e64 v57, s[0:1], 0, v41, s[0:1]
	s_mov_b32 s0, 0x144000
	s_nop 0
	v_add_co_u32_e64 v60, s[0:1], s0, v40
	global_load_dwordx4 v[52:55], v[52:53], off offset:2560
	s_nop 0
	global_load_dwordx4 v[56:59], v[56:57], off offset:2816
	v_addc_co_u32_e64 v61, s[0:1], 0, v41, s[0:1]
	s_mov_b32 s0, 0x15f000
	s_nop 0
	v_add_co_u32_e64 v64, s[0:1], s0, v40
	s_nop 1
	v_addc_co_u32_e64 v65, s[0:1], 0, v41, s[0:1]
	s_mov_b32 s0, 0x17a000
	s_nop 0
	v_add_co_u32_e64 v68, s[0:1], s0, v40
	global_load_dwordx4 v[60:63], v[60:61], off offset:3072
	s_nop 0
	global_load_dwordx4 v[64:67], v[64:65], off offset:3328
	v_addc_co_u32_e64 v69, s[0:1], 0, v41, s[0:1]
	s_mov_b32 s0, 0x195000
	s_nop 0
	v_add_co_u32_e64 v40, s[0:1], s0, v40
	s_nop 1
	v_addc_co_u32_e64 v41, s[0:1], 0, v41, s[0:1]
	global_load_dwordx4 v[68:71], v[68:69], off offset:3584
	s_nop 0
	global_load_dwordx4 v[72:75], v[40:41], off offset:3840
	v_lshlrev_b32_e32 v40, 10, v47
	v_sub_u32_e32 v76, v3, v40
	s_waitcnt vmcnt(0)
	v_cndmask_b32_e32 v4, 0, v4, vcc
	v_cndmask_b32_e32 v5, 0, v5, vcc
	ds_write2_b32 v163, v4, v5 offset1:1
	v_cndmask_b32_e32 v4, 0, v6, vcc
	v_cndmask_b32_e32 v5, 0, v7, vcc
	ds_write2_b32 v163, v4, v5 offset0:2 offset1:3
	v_cndmask_b32_e32 v4, 0, v8, vcc
	v_cndmask_b32_e32 v5, 0, v9, vcc
	v_add_u32_e32 v6, 0x410, v163
	ds_write2_b32 v6, v4, v5 offset1:1
	v_cndmask_b32_e32 v4, 0, v10, vcc
	v_cndmask_b32_e32 v5, 0, v11, vcc
	v_add_u32_e32 v6, 0x418, v163
	ds_write2_b32 v6, v4, v5 offset1:1
	v_cndmask_b32_e32 v4, 0, v12, vcc
	v_cndmask_b32_e32 v5, 0, v13, vcc
	v_add_u32_e32 v6, 0x820, v163
	ds_write2_b32 v6, v4, v5 offset1:1
	v_cndmask_b32_e32 v4, 0, v14, vcc
	v_cndmask_b32_e32 v5, 0, v15, vcc
	v_add_u32_e32 v6, 0x828, v163
	ds_write2_b32 v6, v4, v5 offset1:1
	v_cndmask_b32_e32 v4, 0, v16, vcc
	v_cndmask_b32_e32 v5, 0, v17, vcc
	v_add_u32_e32 v6, 0xc30, v163
	ds_write2_b32 v6, v4, v5 offset1:1
	v_cndmask_b32_e32 v4, 0, v18, vcc
	v_cndmask_b32_e32 v5, 0, v19, vcc
	v_add_u32_e32 v6, 0xc38, v163
	ds_write2_b32 v6, v4, v5 offset1:1
	v_cndmask_b32_e32 v4, 0, v20, vcc
	v_cndmask_b32_e32 v5, 0, v21, vcc
	v_add_u32_e32 v6, 0x1040, v163
	ds_write2_b32 v6, v4, v5 offset1:1
	v_cndmask_b32_e32 v4, 0, v22, vcc
	v_cndmask_b32_e32 v5, 0, v23, vcc
	v_add_u32_e32 v6, 0x1048, v163
	ds_write2_b32 v6, v4, v5 offset1:1
	v_cndmask_b32_e32 v4, 0, v24, vcc
	v_cndmask_b32_e32 v5, 0, v25, vcc
	v_add_u32_e32 v6, 0x1450, v163
	ds_write2_b32 v6, v4, v5 offset1:1
	v_cndmask_b32_e32 v4, 0, v26, vcc
	v_cndmask_b32_e32 v5, 0, v27, vcc
	v_add_u32_e32 v6, 0x1458, v163
	ds_write2_b32 v6, v4, v5 offset1:1
	v_cndmask_b32_e32 v4, 0, v28, vcc
	v_cndmask_b32_e32 v5, 0, v29, vcc
	v_add_u32_e32 v6, 0x1860, v163
	ds_write2_b32 v6, v4, v5 offset1:1
	v_cndmask_b32_e32 v4, 0, v30, vcc
	v_cndmask_b32_e32 v5, 0, v31, vcc
	v_add_u32_e32 v6, 0x1868, v163
	ds_write2_b32 v6, v4, v5 offset1:1
	v_cndmask_b32_e32 v4, 0, v32, vcc
	v_cndmask_b32_e32 v5, 0, v33, vcc
	v_add_u32_e32 v6, 0x1c70, v163
	ds_write2_b32 v6, v4, v5 offset1:1
	v_cndmask_b32_e32 v4, 0, v34, vcc
	v_cndmask_b32_e32 v5, 0, v35, vcc
	v_add_u32_e32 v6, 0x1c78, v163
	ds_write2_b32 v6, v4, v5 offset1:1
	v_cndmask_b32_e32 v4, 0, v36, vcc
	v_cndmask_b32_e32 v5, 0, v37, vcc
	v_add_u32_e32 v6, 0x2080, v163
	ds_write2_b32 v6, v4, v5 offset1:1
	v_cndmask_b32_e32 v4, 0, v38, vcc
	v_cndmask_b32_e32 v5, 0, v39, vcc
	v_add_u32_e32 v6, 0x2088, v163
	ds_write2_b32 v6, v4, v5 offset1:1
	v_cndmask_b32_e32 v4, 0, v48, vcc
	v_cndmask_b32_e32 v5, 0, v49, vcc
	v_add_u32_e32 v6, 0x2490, v163
	ds_write2_b32 v6, v4, v5 offset1:1
	v_cndmask_b32_e32 v4, 0, v50, vcc
	v_cndmask_b32_e32 v5, 0, v51, vcc
	v_add_u32_e32 v6, 0x2498, v163
	ds_write2_b32 v6, v4, v5 offset1:1
	v_cndmask_b32_e32 v4, 0, v52, vcc
	v_cndmask_b32_e32 v5, 0, v53, vcc
	v_add_u32_e32 v6, 0x28a0, v163
	ds_write2_b32 v6, v4, v5 offset1:1
	v_cndmask_b32_e32 v4, 0, v54, vcc
	v_cndmask_b32_e32 v5, 0, v55, vcc
	v_add_u32_e32 v6, 0x28a8, v163
	ds_write2_b32 v6, v4, v5 offset1:1
	v_cndmask_b32_e32 v4, 0, v56, vcc
	v_cndmask_b32_e32 v5, 0, v57, vcc
	v_add_u32_e32 v6, 0x2cb0, v163
	ds_write2_b32 v6, v4, v5 offset1:1
	v_cndmask_b32_e32 v4, 0, v58, vcc
	v_cndmask_b32_e32 v5, 0, v59, vcc
	v_add_u32_e32 v6, 0x2cb8, v163
	ds_write2_b32 v6, v4, v5 offset1:1
	v_cndmask_b32_e32 v4, 0, v60, vcc
	v_cndmask_b32_e32 v5, 0, v61, vcc
	v_add_u32_e32 v6, 0x30c0, v163
	ds_write2_b32 v6, v4, v5 offset1:1
	v_cndmask_b32_e32 v4, 0, v62, vcc
	v_cndmask_b32_e32 v5, 0, v63, vcc
	v_add_u32_e32 v6, 0x30c8, v163
	ds_write2_b32 v6, v4, v5 offset1:1
	v_cndmask_b32_e32 v4, 0, v64, vcc
	v_cndmask_b32_e32 v5, 0, v65, vcc
	v_add_u32_e32 v6, 0x34d0, v163
	ds_write2_b32 v6, v4, v5 offset1:1
	v_cndmask_b32_e32 v4, 0, v66, vcc
	v_cndmask_b32_e32 v5, 0, v67, vcc
	v_add_u32_e32 v6, 0x34d8, v163
	ds_write2_b32 v6, v4, v5 offset1:1
	v_cndmask_b32_e32 v4, 0, v68, vcc
	v_cndmask_b32_e32 v5, 0, v69, vcc
	v_add_u32_e32 v6, 0x38e0, v163
	ds_write2_b32 v6, v4, v5 offset1:1
	v_cndmask_b32_e32 v4, 0, v70, vcc
	v_cndmask_b32_e32 v5, 0, v71, vcc
	v_add_u32_e32 v6, 0x38e8, v163
	ds_write2_b32 v6, v4, v5 offset1:1
	v_cndmask_b32_e32 v4, 0, v72, vcc
	v_cndmask_b32_e32 v5, 0, v73, vcc
	v_add_u32_e32 v6, 0x3cf0, v163
	ds_write2_b32 v6, v4, v5 offset1:1
	v_cndmask_b32_e32 v4, 0, v74, vcc
	v_cndmask_b32_e32 v5, 0, v75, vcc
	v_add_u32_e32 v6, 0x3cf8, v163
	ds_write2_b32 v6, v4, v5 offset1:1
	v_add_u32_e32 v40, 0x400, v165
	ds_read2_b32 v[24:25], v165 offset1:8
	ds_read2_b32 v[26:27], v165 offset0:65 offset1:73
	ds_read2_b32 v[28:29], v165 offset0:130 offset1:138
	ds_read2_b32 v[30:31], v165 offset0:195 offset1:203
	ds_read2_b32 v[32:33], v40 offset0:4 offset1:12
	ds_read2_b32 v[34:35], v40 offset0:69 offset1:77
	ds_read2_b32 v[36:37], v40 offset0:134 offset1:142
	ds_read2_b32 v[38:39], v40 offset0:199 offset1:207
	ds_read2_b32 v[8:9], v165 offset0:16 offset1:24
	ds_read2_b32 v[10:11], v165 offset0:81 offset1:89
	ds_read2_b32 v[12:13], v165 offset0:146 offset1:154
	ds_read2_b32 v[14:15], v165 offset0:211 offset1:219
	ds_read2_b32 v[16:17], v40 offset0:20 offset1:28
	ds_read2_b32 v[18:19], v40 offset0:85 offset1:93
	ds_read2_b32 v[20:21], v40 offset0:150 offset1:158
	ds_read2_b32 v[22:23], v40 offset0:215 offset1:223
	v_or_b32_e32 v6, v77, v164
	v_ashrrev_i32_e32 v77, 31, v76
	v_lshl_add_u64 v[4:5], v[76:77], 1, v[120:121]
	v_cmp_gt_i32_e32 vcc, s33, v6
	s_and_saveexec_b64 s[0:1], vcc
	s_cbranch_execz .LBB0_102
	v_ashrrev_i32_e32 v7, 31, v6
	v_lshlrev_b64 v[52:53], 11, v[6:7]
	s_waitcnt lgkmcnt(14)
	v_cvt_pk_bf16_f32 v48, v24, v26
	s_waitcnt lgkmcnt(12)
	v_cvt_pk_bf16_f32 v49, v28, v30
	s_waitcnt lgkmcnt(10)
	v_cvt_pk_bf16_f32 v50, v32, v34
	s_waitcnt lgkmcnt(8)
	v_cvt_pk_bf16_f32 v51, v36, v38
	v_lshl_add_u64 v[52:53], v[4:5], 0, v[52:53]
	global_store_dwordx4 v[52:53], v[48:51], off
